# k_fused: tri-bias loads skipped for dead (masked) key tiles, vmcnt(4) instead of vmcnt(0) before chunk-1 QK
# speedup vs baseline: 1.0340x; 1.0178x over previous
.LBB1_11:
	v_lshl_add_u64 v[4:5], v[218:219], 0, s[36:37]
	v_add_co_u32_e32 v8, vcc, s33, v4
	v_lshl_add_u64 v[6:7], v[4:5], 0, s[34:35]
	s_nop 0
	v_addc_co_u32_e32 v9, vcc, 0, v5, vcc
	s_and_b64 vcc, exec, s[10:11]
	s_cbranch_vccz .Ltri1_k5
	global_load_dwordx4 v[186:189], v[4:5], off offset:16
	global_load_dwordx4 v[190:193], v[4:5], off
.Ltri1_k5:
	s_and_b64 vcc, exec, s[8:9]
	s_cbranch_vccz .Ltri1_k6
	global_load_dwordx4 v[178:181], v[4:5], off offset:2064
	global_load_dwordx4 v[182:185], v[4:5], off offset:2048
.Ltri1_k6:
	s_and_b64 vcc, exec, s[14:15]
	s_cbranch_vccz .Ltri1_k7
	global_load_dwordx4 v[170:173], v[8:9], off
	global_load_dwordx4 v[174:177], v[6:7], off offset:16
.Ltri1_k7:
	s_and_b64 vcc, exec, s[12:13]
	s_cbranch_vccz .Ltri1_done
	v_lshl_add_u64 v[4:5], v[4:5], 0, s[40:41]
	global_load_dwordx4 v[162:165], v[8:9], off offset:2048
	global_load_dwordx4 v[166:169], v[4:5], off offset:16
.Ltri1_done:
	s_cmp_lg_u32 s36, 0x60000
	s_cselect_b64 s[52:53], -1, 0
	s_cmp_eq_u32 s36, 0x60000
	s_cselect_b32 s23, s27, s55
	s_cselect_b32 s22, s26, s54
	s_setprio 0
	v_readfirstlane_b32 s24, v224
	s_mov_b32 m0, s24
	v_readfirstlane_b32 s24, v225
	global_load_lds_dwordx4 v223, s[22:23]
	s_mov_b32 m0, s24
	v_readfirstlane_b32 s24, v213
	global_load_lds_dwordx4 v210, s[22:23]
	s_mov_b32 m0, s24
	v_readfirstlane_b32 s24, v215
	global_load_lds_dwordx4 v212, s[22:23]
	s_mov_b32 m0, s24
	v_cndmask_b32_e64 v1, 0, 1, s[2:3]
	global_load_lds_dwordx4 v214, s[22:23]
	v_mov_b32_e32 v243, 0xff800000
	v_cmp_ne_u32_e64 s[22:23], 1, v1
	s_andn2_b64 vcc, exec, s[2:3]
	v_mov_b32_e32 v1, 0xff800000
	s_cbranch_vccz .LBB1_64
	s_and_b64 vcc, exec, s[22:23]
	s_cbranch_vccz .LBB1_65

.LBB1_37:
	v_lshl_add_u64 v[4:5], v[216:217], 0, s[36:37]
	v_add_co_u32_e32 v8, vcc, 0x20000, v4
	v_lshl_add_u64 v[6:7], v[4:5], 0, s[44:45]
	s_nop 0
	v_addc_co_u32_e32 v9, vcc, 0, v5, vcc
	s_and_b64 vcc, exec, s[2:3]
	s_cbranch_vccz .Ltri0_k1
	global_load_dwordx4 v[190:193], v[8:9], off
	global_load_dwordx4 v[186:189], v[6:7], off offset:16
.Ltri0_k1:
	s_and_b64 vcc, exec, s[0:1]
	s_cbranch_vccz .Ltri0_k2
	v_lshl_add_u64 v[6:7], v[4:5], 0, s[46:47]
	global_load_dwordx4 v[182:185], v[8:9], off offset:2048
	global_load_dwordx4 v[178:181], v[6:7], off offset:16
.Ltri0_k2:
	v_add_co_u32_e32 v8, vcc, s57, v4
	v_lshl_add_u64 v[6:7], v[4:5], 0, s[48:49]
	s_nop 0
	v_addc_co_u32_e32 v9, vcc, 0, v5, vcc
	s_and_b64 vcc, exec, s[6:7]
	s_cbranch_vccz .Ltri0_k3
	global_load_dwordx4 v[170:173], v[8:9], off
	global_load_dwordx4 v[174:177], v[6:7], off offset:16
.Ltri0_k3:
	s_and_b64 vcc, exec, s[4:5]
	s_cbranch_vccz .LBB1_38
	v_lshl_add_u64 v[4:5], v[4:5], 0, s[50:51]
	global_load_dwordx4 v[162:165], v[8:9], off offset:2048
	global_load_dwordx4 v[166:169], v[4:5], off offset:16

.LBB1_71:
	s_waitcnt vmcnt(4)
	ds_read_b128 v[4:7], v226 offset:512
	ds_read_b128 v[8:11], v226 offset:528
	ds_read_b128 v[12:15], v206 offset:40960
	ds_read_b128 v[114:117], v226 offset:544
	ds_read_b128 v[118:121], v226 offset:560
	s_waitcnt lgkmcnt(0)
	v_fma_mix_f32 v66, v190, s42, v4 op_sel:[0,0,0] op_sel_hi:[1,0,0]
	v_fma_mix_f32 v67, v190, s42, v5 op_sel:[1,0,0] op_sel_hi:[1,0,0]
	v_fma_mix_f32 v68, v191, s42, v6 op_sel:[0,0,0] op_sel_hi:[1,0,0]
	v_fma_mix_f32 v69, v191, s42, v7 op_sel:[1,0,0] op_sel_hi:[1,0,0]
	v_fma_mix_f32 v70, v192, s42, v8 op_sel:[0,0,0] op_sel_hi:[1,0,0]
	v_fma_mix_f32 v71, v192, s42, v9 op_sel:[1,0,0] op_sel_hi:[1,0,0]
	v_fma_mix_f32 v72, v193, s42, v10 op_sel:[0,0,0] op_sel_hi:[1,0,0]
	v_fma_mix_f32 v73, v193, s42, v11 op_sel:[1,0,0] op_sel_hi:[1,0,0]
	s_nop 1
	ds_read_b128 v[4:7], v206 offset:41984
	v_fma_mix_f32 v74, v186, s42, v114 op_sel:[0,0,0] op_sel_hi:[1,0,0]
	v_fma_mix_f32 v75, v186, s42, v115 op_sel:[1,0,0] op_sel_hi:[1,0,0]
	v_fma_mix_f32 v76, v187, s42, v116 op_sel:[0,0,0] op_sel_hi:[1,0,0]
	v_fma_mix_f32 v77, v187, s42, v117 op_sel:[1,0,0] op_sel_hi:[1,0,0]
	v_fma_mix_f32 v78, v188, s42, v118 op_sel:[0,0,0] op_sel_hi:[1,0,0]
	v_fma_mix_f32 v79, v188, s42, v119 op_sel:[1,0,0] op_sel_hi:[1,0,0]
	v_fma_mix_f32 v80, v189, s42, v120 op_sel:[0,0,0] op_sel_hi:[1,0,0]
	v_fma_mix_f32 v81, v189, s42, v121 op_sel:[1,0,0] op_sel_hi:[1,0,0]
	s_nop 1
	s_nop 0
	v_mfma_f32_32x32x16_f16 v[66:81], v[12:15], v[198:201], v[66:81]
	s_waitcnt lgkmcnt(0)
	v_mfma_f32_32x32x16_f16 v[66:81], v[4:7], v[202:205], v[66:81]
	v_cndmask_b32_e64 v1, 0, 1, s[8:9]
	v_cmp_ne_u32_e64 s[20:21], 1, v1
	s_andn2_b64 vcc, exec, s[8:9]
	s_cbranch_vccnz .LBB1_34
.LBB1_72:
	s_waitcnt vmcnt(4)
	ds_read_b128 v[4:7], v226 offset:640
	ds_read_b128 v[8:11], v226 offset:656
	ds_read_b128 v[12:15], v206 offset:43008
	ds_read_b128 v[114:117], v226 offset:672
	ds_read_b128 v[118:121], v226 offset:688
	s_waitcnt lgkmcnt(0)
	v_fma_mix_f32 v50, v182, s42, v4 op_sel:[0,0,0] op_sel_hi:[1,0,0]
	v_fma_mix_f32 v51, v182, s42, v5 op_sel:[1,0,0] op_sel_hi:[1,0,0]
	v_fma_mix_f32 v52, v183, s42, v6 op_sel:[0,0,0] op_sel_hi:[1,0,0]
	v_fma_mix_f32 v53, v183, s42, v7 op_sel:[1,0,0] op_sel_hi:[1,0,0]
	v_fma_mix_f32 v54, v184, s42, v8 op_sel:[0,0,0] op_sel_hi:[1,0,0]
	v_fma_mix_f32 v55, v184, s42, v9 op_sel:[1,0,0] op_sel_hi:[1,0,0]
	v_fma_mix_f32 v56, v185, s42, v10 op_sel:[0,0,0] op_sel_hi:[1,0,0]
	v_fma_mix_f32 v57, v185, s42, v11 op_sel:[1,0,0] op_sel_hi:[1,0,0]
	s_nop 1
	ds_read_b128 v[4:7], v206 offset:44032
	v_fma_mix_f32 v58, v178, s42, v114 op_sel:[0,0,0] op_sel_hi:[1,0,0]
	v_fma_mix_f32 v59, v178, s42, v115 op_sel:[1,0,0] op_sel_hi:[1,0,0]
	v_fma_mix_f32 v60, v179, s42, v116 op_sel:[0,0,0] op_sel_hi:[1,0,0]
	v_fma_mix_f32 v61, v179, s42, v117 op_sel:[1,0,0] op_sel_hi:[1,0,0]
	v_fma_mix_f32 v62, v180, s42, v118 op_sel:[0,0,0] op_sel_hi:[1,0,0]
	v_fma_mix_f32 v63, v180, s42, v119 op_sel:[1,0,0] op_sel_hi:[1,0,0]
	v_fma_mix_f32 v64, v181, s42, v120 op_sel:[0,0,0] op_sel_hi:[1,0,0]
	v_fma_mix_f32 v65, v181, s42, v121 op_sel:[1,0,0] op_sel_hi:[1,0,0]
	s_nop 1
	s_nop 0
	v_mfma_f32_32x32x16_f16 v[50:65], v[12:15], v[198:201], v[50:65]
	s_waitcnt lgkmcnt(0)
	v_mfma_f32_32x32x16_f16 v[50:65], v[4:7], v[202:205], v[50:65]
	v_cndmask_b32_e64 v1, 0, 1, s[14:15]
	v_cmp_ne_u32_e64 s[22:23], 1, v1
	s_andn2_b64 vcc, exec, s[14:15]
	s_cbranch_vccnz .LBB1_35
.LBB1_73:
	s_waitcnt vmcnt(4)
	ds_read_b128 v[4:7], v226 offset:768
	ds_read_b128 v[8:11], v226 offset:784
	ds_read_b128 v[12:15], v206 offset:45056
	ds_read_b128 v[114:117], v226 offset:800
	ds_read_b128 v[118:121], v226 offset:816
	s_waitcnt lgkmcnt(0)
	v_fma_mix_f32 v34, v170, s42, v4 op_sel:[0,0,0] op_sel_hi:[1,0,0]
	v_fma_mix_f32 v35, v170, s42, v5 op_sel:[1,0,0] op_sel_hi:[1,0,0]
	v_fma_mix_f32 v36, v171, s42, v6 op_sel:[0,0,0] op_sel_hi:[1,0,0]
	v_fma_mix_f32 v37, v171, s42, v7 op_sel:[1,0,0] op_sel_hi:[1,0,0]
	v_fma_mix_f32 v38, v172, s42, v8 op_sel:[0,0,0] op_sel_hi:[1,0,0]
	v_fma_mix_f32 v39, v172, s42, v9 op_sel:[1,0,0] op_sel_hi:[1,0,0]
	v_fma_mix_f32 v40, v173, s42, v10 op_sel:[0,0,0] op_sel_hi:[1,0,0]
	v_fma_mix_f32 v41, v173, s42, v11 op_sel:[1,0,0] op_sel_hi:[1,0,0]
	s_nop 1
	ds_read_b128 v[4:7], v206 offset:46080
	v_fma_mix_f32 v42, v174, s42, v114 op_sel:[0,0,0] op_sel_hi:[1,0,0]
	v_fma_mix_f32 v43, v174, s42, v115 op_sel:[1,0,0] op_sel_hi:[1,0,0]
	v_fma_mix_f32 v44, v175, s42, v116 op_sel:[0,0,0] op_sel_hi:[1,0,0]
	v_fma_mix_f32 v45, v175, s42, v117 op_sel:[1,0,0] op_sel_hi:[1,0,0]
	v_fma_mix_f32 v46, v176, s42, v118 op_sel:[0,0,0] op_sel_hi:[1,0,0]
	v_fma_mix_f32 v47, v176, s42, v119 op_sel:[1,0,0] op_sel_hi:[1,0,0]
	v_fma_mix_f32 v48, v177, s42, v120 op_sel:[0,0,0] op_sel_hi:[1,0,0]
	v_fma_mix_f32 v49, v177, s42, v121 op_sel:[1,0,0] op_sel_hi:[1,0,0]
	s_nop 1
	s_nop 0
	v_mfma_f32_32x32x16_f16 v[34:49], v[12:15], v[198:201], v[34:49]
	s_waitcnt lgkmcnt(0)
	v_mfma_f32_32x32x16_f16 v[34:49], v[4:7], v[202:205], v[34:49]
	v_cndmask_b32_e64 v1, 0, 1, s[12:13]
	v_cmp_ne_u32_e64 s[24:25], 1, v1
	s_andn2_b64 vcc, exec, s[12:13]
	s_cbranch_vccnz .LBB1_36
.LBB1_74:
	s_waitcnt vmcnt(4)
	ds_read_b128 v[4:7], v226 offset:896
	ds_read_b128 v[8:11], v226 offset:912
	ds_read_b128 v[12:15], v206 offset:47104
	ds_read_b128 v[114:117], v226 offset:928
	ds_read_b128 v[118:121], v226 offset:944
	s_waitcnt lgkmcnt(0)
	v_fma_mix_f32 v18, v162, s42, v4 op_sel:[0,0,0] op_sel_hi:[1,0,0]
	v_fma_mix_f32 v19, v162, s42, v5 op_sel:[1,0,0] op_sel_hi:[1,0,0]
	v_fma_mix_f32 v20, v163, s42, v6 op_sel:[0,0,0] op_sel_hi:[1,0,0]
	v_fma_mix_f32 v21, v163, s42, v7 op_sel:[1,0,0] op_sel_hi:[1,0,0]
	v_fma_mix_f32 v22, v164, s42, v8 op_sel:[0,0,0] op_sel_hi:[1,0,0]
	v_fma_mix_f32 v23, v164, s42, v9 op_sel:[1,0,0] op_sel_hi:[1,0,0]
	v_fma_mix_f32 v24, v165, s42, v10 op_sel:[0,0,0] op_sel_hi:[1,0,0]
	v_fma_mix_f32 v25, v165, s42, v11 op_sel:[1,0,0] op_sel_hi:[1,0,0]
	s_nop 1
	ds_read_b128 v[4:7], v206 offset:48128
	v_fma_mix_f32 v26, v166, s42, v114 op_sel:[0,0,0] op_sel_hi:[1,0,0]
	v_fma_mix_f32 v27, v166, s42, v115 op_sel:[1,0,0] op_sel_hi:[1,0,0]
	v_fma_mix_f32 v28, v167, s42, v116 op_sel:[0,0,0] op_sel_hi:[1,0,0]
	v_fma_mix_f32 v29, v167, s42, v117 op_sel:[1,0,0] op_sel_hi:[1,0,0]
	v_fma_mix_f32 v30, v168, s42, v118 op_sel:[0,0,0] op_sel_hi:[1,0,0]
	v_fma_mix_f32 v31, v168, s42, v119 op_sel:[1,0,0] op_sel_hi:[1,0,0]
	v_fma_mix_f32 v32, v169, s42, v120 op_sel:[0,0,0] op_sel_hi:[1,0,0]
	v_fma_mix_f32 v33, v169, s42, v121 op_sel:[1,0,0] op_sel_hi:[1,0,0]
	s_nop 1
	s_nop 0
	v_mfma_f32_32x32x16_f16 v[18:33], v[12:15], v[198:201], v[18:33]
	s_waitcnt lgkmcnt(0)
	v_mfma_f32_32x32x16_f16 v[18:33], v[4:7], v[202:205], v[18:33]
	v_cndmask_b32_e64 v1, 0, 1, s[52:53]
	v_cmp_ne_u32_e64 s[16:17], 1, v1
	s_andn2_b64 vcc, exec, s[52:53]
	s_cbranch_vccz .LBB1_37
	s_branch .LBB1_38
